# w_ff2 conversion path: next item's 16 tile loads prefetched into a second register set during the current item
# baseline (speedup 1.0000x reference)
.LBB0_1026:
	s_lshr_b32 s7, s62, 9
	s_mul_hi_u32 s58, s7, 0x2302303
	s_mul_i32 s55, s58, 0xea00
	s_sub_i32 s52, s78, s55
	s_add_i32 s29, s82, s28
	s_cmpk_eq_i32 s26, 0x1c0
	s_cselect_b64 s[56:57], -1, 0
	s_add_i32 s53, s67, s28
	s_lshr_b32 s7, s29, 9
	s_add_i32 s54, s53, s52
	s_mul_hi_u32 s8, s7, 0x2302303
	s_cmpk_gt_i32 s54, 0x4dff
	s_mov_b64 s[40:41], -1
	s_cbranch_scc0 .LBB0_1112
	s_cmpk_gt_u32 s54, 0x59ff
	s_cbranch_scc0 .LBB0_1109
	s_mul_i32 s58, s58, 0x75000
	s_cmpk_gt_u32 s54, 0x69ff
	s_cbranch_scc0 .LBB0_1106
	s_cmpk_gt_u32 s54, 0xa9ff
	s_cbranch_scc0 .LBB0_1031
	s_sub_i32 s7, s62, s55
	s_and_b32 s40, s7, 0xfe00
	s_load_dwordx2 s[50:51], s[0:1], 0x68
	s_add_i32 s49, s40, 0xffff5600
	s_add_i32 s41, s40, 0xffff563c
	s_add_i32 s44, s40, 0xffff5638
	s_add_i32 s45, s40, 0xffff5634
	s_add_i32 s46, s40, 0xffff5630
	s_add_i32 s47, s40, 0xffff562c
	s_add_i32 s48, s40, 0xffff5628
	s_add_i32 s7, s40, 0xffff5624
	s_add_i32 s10, s40, 0xffff5620
	s_add_i32 s11, s40, 0xffff561c
	s_add_i32 s59, s40, 0xffff5618
	s_add_i32 s77, s40, 0xffff5614
	s_add_i32 s89, s40, 0xffff5610
	s_add_i32 s91, s40, 0xffff560c
	s_add_i32 vcc_lo, s40, 0xffff5608
	s_add_i32 vcc_hi, s40, 0xffff5604
	s_add_i32 s40, s26, s49
	s_lshl_b64 s[42:43], s[8:9], 27
	s_add_u32 s42, s71, s42
	s_addc_u32 s43, s23, s43
	s_lshl_b64 s[60:61], s[8:9], 28
	s_waitcnt lgkmcnt(0)
	s_add_u32 s50, s50, s60
	v_add_u32_e32 v8, s26, v67
	s_addc_u32 s51, s51, s61
	v_add_u32_e32 v2, s49, v8
	s_lshl_b32 s49, s63, 2
	s_add_u32 s50, s50, s49
	s_addc_u32 s51, s51, 0
	s_cmp_eq_u32 s26, 0
	s_cbranch_scc0 .Lcv2_warm
	v_lshlrev_b32_e32 v0, 2, v66
	v_ashrrev_i32_e32 v3, 31, v2
	v_lshl_add_u64 v[6:7], s[50:51], 0, v[0:1]
	v_lshlrev_b64 v[2:3], 14, v[2:3]
	v_lshl_add_u64 v[2:3], v[6:7], 0, v[2:3]
	v_mov_b32_e32 v250, 0x10000
	v_mad_u64_u32 v[252:253], s[98:99], v250, 16, v[2:3]
	global_load_dwordx4 v[38:41], v[2:3], off nt
	v_add_u32_e32 v2, vcc_hi, v8
	v_ashrrev_i32_e32 v3, 31, v2
	v_lshlrev_b64 v[2:3], 14, v[2:3]
	v_lshl_add_u64 v[2:3], v[6:7], 0, v[2:3]
	global_load_dwordx4 v[42:45], v[2:3], off nt
	v_add_u32_e32 v2, vcc_lo, v8
	v_ashrrev_i32_e32 v3, 31, v2
	v_lshlrev_b64 v[2:3], 14, v[2:3]
	v_lshl_add_u64 v[2:3], v[6:7], 0, v[2:3]
	global_load_dwordx4 v[46:49], v[2:3], off nt
	v_add_u32_e32 v2, s91, v8
	v_ashrrev_i32_e32 v3, 31, v2
	v_lshlrev_b64 v[2:3], 14, v[2:3]
	v_lshl_add_u64 v[2:3], v[6:7], 0, v[2:3]
	global_load_dwordx4 v[50:53], v[2:3], off nt
	v_add_u32_e32 v2, s89, v8
	v_ashrrev_i32_e32 v3, 31, v2
	v_lshlrev_b64 v[2:3], 14, v[2:3]
	v_lshl_add_u64 v[2:3], v[6:7], 0, v[2:3]
	global_load_dwordx4 v[54:57], v[2:3], off nt
	v_add_u32_e32 v2, s77, v8
	v_ashrrev_i32_e32 v3, 31, v2
	v_lshlrev_b64 v[2:3], 14, v[2:3]
	v_lshl_add_u64 v[2:3], v[6:7], 0, v[2:3]
	global_load_dwordx4 v[62:65], v[2:3], off nt
	v_add_u32_e32 v2, s59, v8
	v_ashrrev_i32_e32 v3, 31, v2
	v_lshlrev_b64 v[2:3], 14, v[2:3]
	v_lshl_add_u64 v[2:3], v[6:7], 0, v[2:3]
	global_load_dwordx4 v[58:61], v[2:3], off nt
	v_add_u32_e32 v2, s11, v8
	v_ashrrev_i32_e32 v3, 31, v2
	v_lshlrev_b64 v[2:3], 14, v[2:3]
	v_lshl_add_u64 v[2:3], v[6:7], 0, v[2:3]
	global_load_dwordx4 v[34:37], v[2:3], off nt
	v_add_u32_e32 v2, s10, v8
	v_ashrrev_i32_e32 v3, 31, v2
	v_lshlrev_b64 v[2:3], 14, v[2:3]
	v_lshl_add_u64 v[2:3], v[6:7], 0, v[2:3]
	global_load_dwordx4 v[30:33], v[2:3], off nt
	v_add_u32_e32 v2, s7, v8
	v_ashrrev_i32_e32 v3, 31, v2
	v_lshlrev_b64 v[2:3], 14, v[2:3]
	v_lshl_add_u64 v[2:3], v[6:7], 0, v[2:3]
	global_load_dwordx4 v[26:29], v[2:3], off nt
	v_add_u32_e32 v2, s48, v8
	v_ashrrev_i32_e32 v3, 31, v2
	v_lshlrev_b64 v[2:3], 14, v[2:3]
	v_lshl_add_u64 v[2:3], v[6:7], 0, v[2:3]
	global_load_dwordx4 v[22:25], v[2:3], off nt
	v_add_u32_e32 v2, s47, v8
	v_ashrrev_i32_e32 v3, 31, v2
	v_lshlrev_b64 v[2:3], 14, v[2:3]
	v_lshl_add_u64 v[2:3], v[6:7], 0, v[2:3]
	global_load_dwordx4 v[18:21], v[2:3], off nt
	v_add_u32_e32 v2, s46, v8
	v_ashrrev_i32_e32 v3, 31, v2
	v_lshlrev_b64 v[2:3], 14, v[2:3]
	v_lshl_add_u64 v[2:3], v[6:7], 0, v[2:3]
	global_load_dwordx4 v[14:17], v[2:3], off nt
	v_add_u32_e32 v2, s45, v8
	v_ashrrev_i32_e32 v3, 31, v2
	v_lshlrev_b64 v[2:3], 14, v[2:3]
	v_lshl_add_u64 v[2:3], v[6:7], 0, v[2:3]
	global_load_dwordx4 v[10:13], v[2:3], off nt
	v_add_u32_e32 v2, s44, v8
	v_add_u32_e32 v8, s41, v8
	v_ashrrev_i32_e32 v3, 31, v2
	v_ashrrev_i32_e32 v9, 31, v8
	v_lshlrev_b64 v[2:3], 14, v[2:3]
	v_lshlrev_b64 v[8:9], 14, v[8:9]
	v_lshl_add_u64 v[2:3], v[6:7], 0, v[2:3]
	v_lshl_add_u64 v[6:7], v[6:7], 0, v[8:9]
	global_load_dwordx4 v[2:5], v[2:3], off nt
	s_mov_b32 s41, s9
	global_load_dwordx4 v[6:9], v[6:7], off nt
	s_branch .Lcv2_go
.Lcv2_warm:
	s_mov_b32 s41, s9
	s_waitcnt vmcnt(8)
	v_mov_b64_e32 v[38:39], v[140:141]
	v_mov_b64_e32 v[40:41], v[142:143]
	v_mov_b64_e32 v[42:43], v[144:145]
	v_mov_b64_e32 v[44:45], v[146:147]
	v_mov_b64_e32 v[46:47], v[148:149]
	v_mov_b64_e32 v[48:49], v[150:151]
	v_mov_b64_e32 v[50:51], v[152:153]
	v_mov_b64_e32 v[52:53], v[154:155]
	v_mov_b64_e32 v[54:55], v[156:157]
	v_mov_b64_e32 v[56:57], v[158:159]
	v_mov_b64_e32 v[62:63], v[160:161]
	v_mov_b64_e32 v[64:65], v[162:163]
	v_mov_b64_e32 v[58:59], v[164:165]
	v_mov_b64_e32 v[60:61], v[166:167]
	v_mov_b64_e32 v[34:35], v[168:169]
	v_mov_b64_e32 v[36:37], v[170:171]
	v_mov_b64_e32 v[30:31], v[172:173]
	v_mov_b64_e32 v[32:33], v[174:175]
	v_mov_b64_e32 v[26:27], v[176:177]
	v_mov_b64_e32 v[28:29], v[178:179]
	v_mov_b64_e32 v[22:23], v[180:181]
	v_mov_b64_e32 v[24:25], v[182:183]
	v_mov_b64_e32 v[18:19], v[184:185]
	v_mov_b64_e32 v[20:21], v[186:187]
	v_mov_b64_e32 v[14:15], v[188:189]
	v_mov_b64_e32 v[16:17], v[190:191]
	v_mov_b64_e32 v[10:11], v[192:193]
	v_mov_b64_e32 v[12:13], v[194:195]
	v_mov_b64_e32 v[2:3], v[196:197]
	v_mov_b64_e32 v[4:5], v[198:199]
	v_mov_b64_e32 v[6:7], v[200:201]
	v_mov_b64_e32 v[8:9], v[202:203]
.Lcv2_go:
	s_cmp_eq_u32 s26, 0x1c0
	s_cbranch_scc1 .Lcv2_nopf
	v_mad_u64_u32 v[248:249], s[98:99], v250, 0, v[252:253]
	global_load_dwordx4 v[140:143], v[248:249], off nt
	v_mad_u64_u32 v[248:249], s[98:99], v250, 1, v[252:253]
	global_load_dwordx4 v[144:147], v[248:249], off nt
	v_mad_u64_u32 v[248:249], s[98:99], v250, 2, v[252:253]
	global_load_dwordx4 v[148:151], v[248:249], off nt
	v_mad_u64_u32 v[248:249], s[98:99], v250, 3, v[252:253]
	global_load_dwordx4 v[152:155], v[248:249], off nt
	v_mad_u64_u32 v[248:249], s[98:99], v250, 4, v[252:253]
	global_load_dwordx4 v[156:159], v[248:249], off nt
	v_mad_u64_u32 v[248:249], s[98:99], v250, 5, v[252:253]
	global_load_dwordx4 v[160:163], v[248:249], off nt
	v_mad_u64_u32 v[248:249], s[98:99], v250, 6, v[252:253]
	global_load_dwordx4 v[164:167], v[248:249], off nt
	v_mad_u64_u32 v[248:249], s[98:99], v250, 7, v[252:253]
	global_load_dwordx4 v[168:171], v[248:249], off nt
	v_mad_u64_u32 v[248:249], s[98:99], v250, 8, v[252:253]
	global_load_dwordx4 v[172:175], v[248:249], off nt
	v_mad_u64_u32 v[248:249], s[98:99], v250, 9, v[252:253]
	global_load_dwordx4 v[176:179], v[248:249], off nt
	v_mad_u64_u32 v[248:249], s[98:99], v250, 10, v[252:253]
	global_load_dwordx4 v[180:183], v[248:249], off nt
	v_mad_u64_u32 v[248:249], s[98:99], v250, 11, v[252:253]
	global_load_dwordx4 v[184:187], v[248:249], off nt
	v_mad_u64_u32 v[248:249], s[98:99], v250, 12, v[252:253]
	global_load_dwordx4 v[188:191], v[248:249], off nt
	v_mad_u64_u32 v[248:249], s[98:99], v250, 13, v[252:253]
	global_load_dwordx4 v[192:195], v[248:249], off nt
	v_mad_u64_u32 v[248:249], s[98:99], v250, 14, v[252:253]
	global_load_dwordx4 v[196:199], v[248:249], off nt
	v_mad_u64_u32 v[248:249], s[98:99], v250, 15, v[252:253]
	global_load_dwordx4 v[200:203], v[248:249], off nt
	v_mad_u64_u32 v[252:253], s[98:99], v250, 16, v[252:253]
.Lcv2_nopf:
	s_waitcnt vmcnt(31)
	v_cvt_pk_bf16_f32 v0, v38, v38
	s_lshl_b64 s[10:11], s[40:41], 1
	v_lshlrev_b32_e32 v108, 16, v0
	ds_write_b32 v69, v108
	v_cvt_pk_bf16_f32 v0, v39, v39
	v_pk_fma_f32 v[38:39], v[38:39], 0, v[106:107] op_sel_hi:[1,0,1]
	v_lshlrev_b32_e32 v109, 16, v0
	ds_write_b32 v69, v109 offset:4
	v_cvt_pk_bf16_f32 v0, v40, v40
	v_pk_add_f32 v[108:109], v[100:101], v[108:109]
	v_lshlrev_b32_e32 v110, 16, v0
	ds_write_b32 v69, v110 offset:8
	v_cvt_pk_bf16_f32 v0, v41, v41
	s_waitcnt vmcnt(30)
	v_pk_fma_f32 v[38:39], v[42:43], 0, v[38:39] op_sel_hi:[1,0,1]
	v_lshlrev_b32_e32 v111, 16, v0
	ds_write_b32 v69, v111 offset:12
	v_cvt_pk_bf16_f32 v0, v42, v42
	v_pk_add_f32 v[110:111], v[102:103], v[110:111]
	v_lshlrev_b32_e32 v114, 16, v0
	ds_write_b32 v69, v114 offset:1040
	v_cvt_pk_bf16_f32 v0, v43, v43
	s_waitcnt vmcnt(29)
	v_pk_fma_f32 v[38:39], v[46:47], 0, v[38:39] op_sel_hi:[1,0,1]
	v_lshlrev_b32_e32 v115, 16, v0
	ds_write_b32 v69, v115 offset:1044
	v_pk_add_f32 v[108:109], v[108:109], v[114:115]
	v_cvt_pk_bf16_f32 v0, v44, v44
	s_waitcnt vmcnt(27)
	v_mul_f32_e32 v113, 0, v55
	v_lshlrev_b32_e32 v114, 16, v0
	ds_write_b32 v69, v114 offset:1048
	v_cvt_pk_bf16_f32 v0, v45, v45
	v_pk_fma_f32 v[38:39], v[50:51], 0, v[38:39] op_sel_hi:[1,0,1]
	v_lshlrev_b32_e32 v115, 16, v0
	ds_write_b32 v69, v115 offset:1052
	v_pk_add_f32 v[110:111], v[110:111], v[114:115]
	v_cvt_pk_bf16_f32 v0, v46, v46
	v_pk_fma_f32 v[40:41], v[40:41], 0, v[104:105] op_sel_hi:[1,0,1]
	v_lshlrev_b32_e32 v114, 16, v0
	ds_write_b32 v69, v114 offset:2080
	v_cvt_pk_bf16_f32 v0, v47, v47
	v_pk_fma_f32 v[40:41], v[44:45], 0, v[40:41] op_sel_hi:[1,0,1]
	v_lshlrev_b32_e32 v115, 16, v0
	ds_write_b32 v69, v115 offset:2084
	v_pk_add_f32 v[108:109], v[108:109], v[114:115]
	v_cvt_pk_bf16_f32 v0, v48, v48
	v_pk_fma_f32 v[40:41], v[48:49], 0, v[40:41] op_sel_hi:[1,0,1]
	v_lshlrev_b32_e32 v114, 16, v0
	ds_write_b32 v69, v114 offset:2088
	v_cvt_pk_bf16_f32 v0, v49, v49
	v_pk_fma_f32 v[40:41], v[52:53], 0, v[40:41] op_sel_hi:[1,0,1]
	v_lshlrev_b32_e32 v115, 16, v0
	ds_write_b32 v69, v115 offset:2092
	v_pk_add_f32 v[110:111], v[110:111], v[114:115]
	v_cvt_pk_bf16_f32 v0, v50, v50
	s_waitcnt vmcnt(23)
	v_mov_b32_e32 v49, v30
	v_lshlrev_b32_e32 v114, 16, v0
	ds_write_b32 v69, v114 offset:3120
	v_cvt_pk_bf16_f32 v0, v51, v51
	s_waitcnt vmcnt(22)
	v_mov_b32_e32 v48, v26
	v_lshlrev_b32_e32 v115, 16, v0
	ds_write_b32 v69, v115 offset:3124
	v_pk_add_f32 v[108:109], v[108:109], v[114:115]
	v_cvt_pk_bf16_f32 v0, v52, v52
	s_waitcnt vmcnt(20)
	v_mov_b32_e32 v52, v18
	v_lshlrev_b32_e32 v114, 16, v0
	ds_write_b32 v69, v114 offset:3128
	v_cvt_pk_bf16_f32 v0, v53, v53
	v_mov_b32_e32 v53, v22
	v_lshlrev_b32_e32 v115, 16, v0
	ds_write_b32 v69, v115 offset:3132
	v_pk_add_f32 v[110:111], v[110:111], v[114:115]
	v_cvt_pk_bf16_f32 v0, v54, v54
	v_pk_mul_f32 v[128:129], v[52:53], 0 op_sel_hi:[1,0]
	v_lshlrev_b32_e32 v114, 16, v0
	ds_write_b32 v69, v114 offset:4160
	v_cvt_pk_bf16_f32 v0, v55, v55
	v_mul_f32_e32 v130, 0, v19
	v_lshlrev_b32_e32 v115, 16, v0
	ds_write_b32 v69, v115 offset:4164
	v_pk_add_f32 v[116:117], v[108:109], v[114:115]
	v_cvt_pk_bf16_f32 v0, v56, v56
	s_waitcnt vmcnt(16)
	v_mov_b32_e32 v136, v6
	v_lshlrev_b32_e32 v108, 16, v0
	ds_write_b32 v69, v108 offset:4168
	v_cvt_pk_bf16_f32 v0, v57, v57
	v_mov_b32_e32 v137, v2
	v_lshlrev_b32_e32 v109, 16, v0
	ds_write_b32 v69, v109 offset:4172
	v_cvt_pk_bf16_f32 v0, v62, v62
	v_pk_add_f32 v[108:109], v[110:111], v[108:109]
	v_lshlrev_b32_e32 v118, 16, v0
	v_mov_b32_e32 v110, v62
	v_mov_b32_e32 v111, v54
	ds_write_b32 v69, v118 offset:5200
	v_cvt_pk_bf16_f32 v0, v63, v63
	v_pk_mul_f32 v[110:111], v[110:111], 0 op_sel_hi:[1,0]
	v_lshlrev_b32_e32 v119, 16, v0
	ds_write_b32 v69, v119 offset:5204
	v_cvt_pk_bf16_f32 v0, v64, v64
	v_mov_b32_e32 v112, v111
	v_lshlrev_b32_e32 v62, 16, v0
	v_mul_f32_e32 v111, 0, v63
	ds_write_b32 v69, v62 offset:5208
	v_cvt_pk_bf16_f32 v0, v65, v65
	v_pk_add_f32 v[112:113], v[112:113], v[38:39]
	v_lshlrev_b32_e32 v63, 16, v0
	ds_write_b32 v69, v63 offset:5212
	v_cvt_pk_bf16_f32 v0, v58, v58
	v_mov_b32_e32 v38, v64
	v_lshlrev_b32_e32 v120, 16, v0
	v_mov_b32_e32 v39, v56
	v_mov_b32_e32 v56, v65
	ds_write_b32 v69, v120 offset:6240
	v_cvt_pk_bf16_f32 v0, v59, v59
	v_pk_mul_f32 v[38:39], v[38:39], 0 op_sel_hi:[1,0]
	v_lshlrev_b32_e32 v121, 16, v0
	v_pk_mul_f32 v[42:43], v[56:57], 0 op_sel_hi:[1,0]
	ds_write_b32 v69, v121 offset:6244
	v_cvt_pk_bf16_f32 v0, v60, v60
	v_mov_b32_e32 v44, v39
	v_lshlrev_b32_e32 v64, 16, v0
	v_mov_b32_e32 v45, v43
	ds_write_b32 v69, v64 offset:6248
	v_cvt_pk_bf16_f32 v0, v61, v61
	v_pk_add_f32 v[40:41], v[44:45], v[40:41]
	v_lshlrev_b32_e32 v65, 16, v0
	ds_write_b32 v69, v65 offset:6252
	v_cvt_pk_bf16_f32 v0, v34, v34
	v_mov_b32_e32 v44, v34
	v_lshlrev_b32_e32 v34, 16, v0
	v_mov_b32_e32 v45, v58
	v_mul_f32_e32 v39, 0, v35
	v_mov_b32_e32 v56, v10
	v_mov_b32_e32 v57, v14
	ds_write_b32 v69, v34 offset:7280
	v_cvt_pk_bf16_f32 v0, v35, v35
	v_pk_mul_f32 v[122:123], v[44:45], 0 op_sel_hi:[1,0]
	v_lshlrev_b32_e32 v35, 16, v0
	v_mov_b32_e32 v44, v36
	v_pk_mul_f32 v[132:133], v[56:57], 0 op_sel_hi:[1,0]
	v_mul_f32_e32 v134, 0, v11
	v_pk_mul_f32 v[136:137], v[136:137], 0 op_sel_hi:[1,0]
	ds_write_b32 v69, v35 offset:7284
	v_cvt_pk_bf16_f32 v0, v36, v36
	v_mul_f32_e32 v36, 0, v7
	v_mov_b32_e32 v126, v129
	v_mov_b32_e32 v129, v130
	v_mov_b32_e32 v130, v133
	v_mov_b32_e32 v133, v134
	v_mov_b32_e32 v134, v137
	v_mov_b32_e32 v137, v36
	v_lshlrev_b32_e32 v36, 16, v0
	v_mov_b32_e32 v45, v60
	v_mov_b32_e32 v60, v37
	ds_write_b32 v69, v36 offset:7288
	v_cvt_pk_bf16_f32 v0, v37, v37
	v_pk_mul_f32 v[46:47], v[60:61], 0 op_sel_hi:[1,0]
	v_lshlrev_b32_e32 v37, 16, v0
	ds_write_b32 v69, v37 offset:7292
	v_cvt_pk_bf16_f32 v0, v30, v30
	v_mul_f32_e32 v61, 0, v31
	v_lshlrev_b32_e32 v30, 16, v0
	ds_write_b32 v69, v30 offset:8320
	v_cvt_pk_bf16_f32 v0, v31, v31
	v_pk_mul_f32 v[124:125], v[48:49], 0 op_sel_hi:[1,0]
	v_lshlrev_b32_e32 v31, 16, v0
	v_mov_b32_e32 v49, v32
	ds_write_b32 v69, v31 offset:8324
	v_cvt_pk_bf16_f32 v0, v32, v32
	v_mov_b32_e32 v51, v33
	v_lshlrev_b32_e32 v32, 16, v0
	ds_write_b32 v69, v32 offset:8328
	v_cvt_pk_bf16_f32 v0, v33, v33
	v_mul_f32_e32 v43, 0, v27
	v_lshlrev_b32_e32 v33, 16, v0
	ds_write_b32 v69, v33 offset:8332
	v_cvt_pk_bf16_f32 v0, v26, v26
	v_mov_b32_e32 v48, v28
	v_lshlrev_b32_e32 v26, 16, v0
	ds_write_b32 v69, v26 offset:9360
	v_cvt_pk_bf16_f32 v0, v27, v27
	v_mov_b32_e32 v50, v29
	v_lshlrev_b32_e32 v27, 16, v0
	ds_write_b32 v69, v27 offset:9364
	v_cvt_pk_bf16_f32 v0, v28, v28
	v_mul_f32_e32 v127, 0, v23
	v_lshlrev_b32_e32 v28, 16, v0
	ds_write_b32 v69, v28 offset:9368
	v_cvt_pk_bf16_f32 v0, v29, v29
	v_mov_b32_e32 v53, v24
	v_lshlrev_b32_e32 v29, 16, v0
	ds_write_b32 v69, v29 offset:9372
	v_cvt_pk_bf16_f32 v0, v22, v22
	v_mov_b32_e32 v55, v25
	v_lshlrev_b32_e32 v22, 16, v0
	ds_write_b32 v69, v22 offset:10400
	v_cvt_pk_bf16_f32 v0, v23, v23
	v_mov_b32_e32 v52, v20
	v_lshlrev_b32_e32 v23, 16, v0
	ds_write_b32 v69, v23 offset:10404
	v_cvt_pk_bf16_f32 v0, v24, v24
	v_mov_b32_e32 v54, v21
	v_lshlrev_b32_e32 v24, 16, v0
	ds_write_b32 v69, v24 offset:10408
	v_cvt_pk_bf16_f32 v0, v25, v25
	v_mul_f32_e32 v131, 0, v15
	v_lshlrev_b32_e32 v25, 16, v0
	ds_write_b32 v69, v25 offset:10412
	v_cvt_pk_bf16_f32 v0, v18, v18
	v_pk_add_f32 v[116:117], v[116:117], v[118:119]
	v_lshlrev_b32_e32 v18, 16, v0
	ds_write_b32 v69, v18 offset:11440
	v_cvt_pk_bf16_f32 v0, v19, v19
	v_mov_b32_e32 v57, v16
	v_lshlrev_b32_e32 v19, 16, v0
	ds_write_b32 v69, v19 offset:11444
	v_cvt_pk_bf16_f32 v0, v20, v20
	v_pk_add_f32 v[116:117], v[116:117], v[120:121]
	v_lshlrev_b32_e32 v20, 16, v0
	ds_write_b32 v69, v20 offset:11448
	v_cvt_pk_bf16_f32 v0, v21, v21
	v_mul_f32_e32 v115, 0, v59
	v_lshlrev_b32_e32 v21, 16, v0
	ds_write_b32 v69, v21 offset:11452
	v_cvt_pk_bf16_f32 v0, v14, v14
	v_mov_b32_e32 v59, v17
	v_lshlrev_b32_e32 v14, 16, v0
	ds_write_b32 v69, v14 offset:12480
	v_cvt_pk_bf16_f32 v0, v15, v15
	v_pk_add_f32 v[116:117], v[116:117], v[34:35]
	v_lshlrev_b32_e32 v15, 16, v0
	ds_write_b32 v69, v15 offset:12484
	v_cvt_pk_bf16_f32 v0, v16, v16
	v_pk_add_f32 v[30:31], v[116:117], v[30:31]
	v_lshlrev_b32_e32 v16, 16, v0
	ds_write_b32 v69, v16 offset:12488
	v_cvt_pk_bf16_f32 v0, v17, v17
	v_pk_add_f32 v[62:63], v[108:109], v[62:63]
	v_lshlrev_b32_e32 v17, 16, v0
	ds_write_b32 v69, v17 offset:12492
	v_cvt_pk_bf16_f32 v0, v10, v10
	v_pk_add_f32 v[26:27], v[30:31], v[26:27]
	v_lshlrev_b32_e32 v10, 16, v0
	ds_write_b32 v69, v10 offset:13520
	v_cvt_pk_bf16_f32 v0, v11, v11
	v_mov_b32_e32 v56, v12
	v_lshlrev_b32_e32 v11, 16, v0
	v_pk_add_f32 v[62:63], v[62:63], v[64:65]
	v_pk_add_f32 v[22:23], v[26:27], v[22:23]
	ds_write_b32 v69, v11 offset:13524
	v_cvt_pk_bf16_f32 v0, v12, v12
	v_mov_b32_e32 v58, v13
	v_lshlrev_b32_e32 v12, 16, v0
	v_pk_add_f32 v[36:37], v[62:63], v[36:37]
	v_pk_add_f32 v[18:19], v[22:23], v[18:19]
	ds_write_b32 v69, v12 offset:13528
	v_cvt_pk_bf16_f32 v0, v13, v13
	v_pk_add_f32 v[32:33], v[36:37], v[32:33]
	v_lshlrev_b32_e32 v13, 16, v0
	v_pk_add_f32 v[14:15], v[18:19], v[14:15]
	ds_write_b32 v69, v13 offset:13532
	v_cvt_pk_bf16_f32 v0, v2, v2
	v_mul_f32_e32 v135, 0, v3
	v_lshlrev_b32_e32 v2, 16, v0
	v_pk_add_f32 v[28:29], v[32:33], v[28:29]
	v_pk_add_f32 v[10:11], v[14:15], v[10:11]
	ds_write_b32 v69, v2 offset:14560
	v_cvt_pk_bf16_f32 v0, v3, v3
	v_pk_add_f32 v[24:25], v[28:29], v[24:25]
	v_lshlrev_b32_e32 v3, 16, v0
	ds_write_b32 v69, v3 offset:14564
	v_pk_add_f32 v[2:3], v[10:11], v[2:3]
	v_cvt_pk_bf16_f32 v0, v4, v4
	v_pk_add_f32 v[20:21], v[24:25], v[20:21]
	v_lshlrev_b32_e32 v10, 16, v0
	ds_write_b32 v69, v10 offset:14568
	v_cvt_pk_bf16_f32 v0, v5, v5
	v_pk_add_f32 v[16:17], v[20:21], v[16:17]
	v_lshlrev_b32_e32 v11, 16, v0
	ds_write_b32 v69, v11 offset:14572
	v_cvt_pk_bf16_f32 v0, v6, v6
	v_pk_add_f32 v[34:35], v[110:111], v[112:113]
	v_lshlrev_b32_e32 v6, 16, v0
	v_mov_b32_e32 v114, v123
	v_pk_add_f32 v[12:13], v[16:17], v[12:13]
	ds_write_b32 v69, v6 offset:15600
	v_cvt_pk_bf16_f32 v0, v7, v7
	v_pk_add_f32 v[34:35], v[114:115], v[34:35]
	v_lshlrev_b32_e32 v7, 16, v0
	v_mov_b32_e32 v123, v39
	v_pk_add_f32 v[12:13], v[12:13], v[10:11]
	v_pk_add_f32 v[10:11], v[2:3], v[6:7]
	ds_write_b32 v69, v7 offset:15604
	v_cvt_pk_bf16_f32 v0, v8, v8
	v_pk_mul_f32 v[44:45], v[44:45], 0 op_sel_hi:[1,0]
	v_lshlrev_b32_e32 v6, 16, v0
	v_pk_add_f32 v[34:35], v[122:123], v[34:35]
	v_mov_b32_e32 v60, v125
	ds_write_b32 v69, v6 offset:15608
	v_cvt_pk_bf16_f32 v0, v9, v9
	v_mov_b32_e32 v39, v42
	v_lshlrev_b32_e32 v7, 16, v0
	v_pk_add_f32 v[34:35], v[60:61], v[34:35]
	v_mov_b32_e32 v60, v8
	v_mov_b32_e32 v61, v4
	v_pk_add_f32 v[2:3], v[12:13], v[6:7]
	ds_write_b32 v69, v7 offset:15612
	v_mov_b32_e32 v4, v9
	v_pk_add_f32 v[6:7], v[38:39], v[40:41]
	v_mov_b32_e32 v8, v45
	v_mov_b32_e32 v9, v47
	v_pk_mul_f32 v[48:49], v[48:49], 0 op_sel_hi:[1,0]
	v_pk_mul_f32 v[50:51], v[50:51], 0 op_sel_hi:[1,0]
	v_pk_add_f32 v[6:7], v[8:9], v[6:7]
	v_mov_b32_e32 v45, v46
	v_pk_add_f32 v[6:7], v[44:45], v[6:7]
	v_mov_b32_e32 v8, v49
	v_mov_b32_e32 v9, v51
	v_pk_mul_f32 v[52:53], v[52:53], 0 op_sel_hi:[1,0]
	v_pk_mul_f32 v[54:55], v[54:55], 0 op_sel_hi:[1,0]
	v_pk_add_f32 v[6:7], v[8:9], v[6:7]
	v_mov_b32_e32 v49, v50
	v_pk_add_f32 v[6:7], v[48:49], v[6:7]
	v_mov_b32_e32 v8, v53
	v_mov_b32_e32 v9, v55
	v_pk_mul_f32 v[56:57], v[56:57], 0 op_sel_hi:[1,0]
	v_pk_mul_f32 v[58:59], v[58:59], 0 op_sel_hi:[1,0]
	v_pk_add_f32 v[6:7], v[8:9], v[6:7]
	v_mov_b32_e32 v53, v54
	v_pk_add_f32 v[6:7], v[52:53], v[6:7]
	v_mov_b32_e32 v8, v57
	v_mov_b32_e32 v9, v59
	v_pk_mul_f32 v[60:61], v[60:61], 0 op_sel_hi:[1,0]
	v_pk_mul_f32 v[4:5], v[4:5], 0 op_sel_hi:[1,0]
	v_pk_add_f32 v[6:7], v[8:9], v[6:7]
	v_mov_b32_e32 v57, v58
	s_waitcnt lgkmcnt(0)
	v_pk_add_f32 v[6:7], v[56:57], v[6:7]
	v_mov_b32_e32 v8, v61
	v_mov_b32_e32 v9, v5
	s_add_u32 s10, s42, s10
	v_pk_add_f32 v[6:7], v[8:9], v[6:7]
	v_mov_b32_e32 v61, v4
	s_addc_u32 s11, s43, s11
	v_lshlrev_b32_e32 v0, 1, v68
	ds_read2_b32 v[8:9], v205 offset1:65
	v_pk_add_f32 v[4:5], v[60:61], v[6:7]
	v_lshl_add_u64 v[6:7], s[10:11], 0, v[0:1]
	s_waitcnt lgkmcnt(0)
	v_cvt_pk_bf16_f32 v12, v8, v9
	ds_read2_b32 v[8:9], v205 offset0:130 offset1:195
	v_add_u32_e32 v0, 0x400, v205
	s_waitcnt lgkmcnt(0)
	v_cvt_pk_bf16_f32 v13, v8, v9
	ds_read2_b32 v[8:9], v0 offset0:4 offset1:69
	s_waitcnt lgkmcnt(0)
	v_cvt_pk_bf16_f32 v14, v8, v9
	ds_read2_b32 v[8:9], v0 offset0:134 offset1:199
	s_waitcnt lgkmcnt(0)
	v_cvt_pk_bf16_f32 v15, v8, v9
	v_lshl_add_u64 v[8:9], v[6:7], 0, v[76:77]
	global_store_dwordx4 v[8:9], v[12:15], off nt
	ds_read2_b32 v[8:9], v205 offset0:8 offset1:73
	v_mov_b32_e32 v125, v43
	s_waitcnt lgkmcnt(0)
	v_cvt_pk_bf16_f32 v12, v8, v9
	ds_read2_b32 v[8:9], v205 offset0:138 offset1:203
	s_waitcnt lgkmcnt(0)
	v_cvt_pk_bf16_f32 v13, v8, v9
	ds_read2_b32 v[8:9], v0 offset0:12 offset1:77
	s_waitcnt lgkmcnt(0)
	v_cvt_pk_bf16_f32 v14, v8, v9
	ds_read2_b32 v[8:9], v0 offset0:142 offset1:207
	s_waitcnt lgkmcnt(0)
	v_cvt_pk_bf16_f32 v15, v8, v9
	v_lshl_add_u64 v[8:9], v[6:7], 0, v[78:79]
	global_store_dwordx4 v[8:9], v[12:15], off nt
	ds_read2_b32 v[8:9], v205 offset0:16 offset1:81
	v_pk_add_f32 v[34:35], v[124:125], v[34:35]
	s_waitcnt lgkmcnt(0)
	v_cvt_pk_bf16_f32 v12, v8, v9
	ds_read2_b32 v[8:9], v205 offset0:146 offset1:211
	s_waitcnt lgkmcnt(0)
	v_cvt_pk_bf16_f32 v13, v8, v9
	ds_read2_b32 v[8:9], v0 offset0:20 offset1:85
	s_waitcnt lgkmcnt(0)
	v_cvt_pk_bf16_f32 v14, v8, v9
	ds_read2_b32 v[8:9], v0 offset0:150 offset1:215
	s_waitcnt lgkmcnt(0)
	v_cvt_pk_bf16_f32 v15, v8, v9
	v_lshl_add_u64 v[8:9], v[6:7], 0, v[80:81]
	global_store_dwordx4 v[8:9], v[12:15], off nt
	ds_read2_b32 v[8:9], v205 offset0:24 offset1:89
	v_pk_add_f32 v[34:35], v[126:127], v[34:35]
	s_waitcnt lgkmcnt(0)
	v_cvt_pk_bf16_f32 v12, v8, v9
	ds_read2_b32 v[8:9], v205 offset0:154 offset1:219
	s_waitcnt lgkmcnt(0)
	v_cvt_pk_bf16_f32 v13, v8, v9
	ds_read2_b32 v[8:9], v0 offset0:28 offset1:93
	s_waitcnt lgkmcnt(0)
	v_cvt_pk_bf16_f32 v14, v8, v9
	ds_read2_b32 v[8:9], v0 offset0:158 offset1:223
	s_waitcnt lgkmcnt(0)
	v_cvt_pk_bf16_f32 v15, v8, v9
	v_lshl_add_u64 v[8:9], v[6:7], 0, v[82:83]
	global_store_dwordx4 v[8:9], v[12:15], off nt
	ds_read2_b32 v[8:9], v205 offset0:32 offset1:97
	v_pk_add_f32 v[34:35], v[128:129], v[34:35]
	s_waitcnt lgkmcnt(0)
	v_cvt_pk_bf16_f32 v12, v8, v9
	ds_read2_b32 v[8:9], v205 offset0:162 offset1:227
	s_waitcnt lgkmcnt(0)
	v_cvt_pk_bf16_f32 v13, v8, v9
	ds_read2_b32 v[8:9], v0 offset0:36 offset1:101
	s_waitcnt lgkmcnt(0)
	v_cvt_pk_bf16_f32 v14, v8, v9
	ds_read2_b32 v[8:9], v0 offset0:166 offset1:231
	s_waitcnt lgkmcnt(0)
	v_cvt_pk_bf16_f32 v15, v8, v9
	v_lshl_add_u64 v[8:9], v[6:7], 0, v[84:85]
	global_store_dwordx4 v[8:9], v[12:15], off nt
	ds_read2_b32 v[8:9], v205 offset0:40 offset1:105
	v_pk_add_f32 v[34:35], v[130:131], v[34:35]
	s_waitcnt lgkmcnt(0)
	v_cvt_pk_bf16_f32 v12, v8, v9
	ds_read2_b32 v[8:9], v205 offset0:170 offset1:235
	s_waitcnt lgkmcnt(0)
	v_cvt_pk_bf16_f32 v13, v8, v9
	ds_read2_b32 v[8:9], v0 offset0:44 offset1:109
	s_waitcnt lgkmcnt(0)
	v_cvt_pk_bf16_f32 v14, v8, v9
	ds_read2_b32 v[8:9], v0 offset0:174 offset1:239
	s_waitcnt lgkmcnt(0)
	v_cvt_pk_bf16_f32 v15, v8, v9
	v_lshl_add_u64 v[8:9], v[6:7], 0, v[86:87]
	global_store_dwordx4 v[8:9], v[12:15], off nt
	ds_read2_b32 v[8:9], v205 offset0:48 offset1:113
	v_pk_add_f32 v[34:35], v[132:133], v[34:35]
	s_waitcnt lgkmcnt(0)
	v_cvt_pk_bf16_f32 v12, v8, v9
	ds_read2_b32 v[8:9], v205 offset0:178 offset1:243
	s_waitcnt lgkmcnt(0)
	v_cvt_pk_bf16_f32 v13, v8, v9
	ds_read2_b32 v[8:9], v0 offset0:52 offset1:117
	s_waitcnt lgkmcnt(0)
	v_cvt_pk_bf16_f32 v14, v8, v9
	ds_read2_b32 v[8:9], v0 offset0:182 offset1:247
	s_waitcnt lgkmcnt(0)
	v_cvt_pk_bf16_f32 v15, v8, v9
	v_lshl_add_u64 v[8:9], v[6:7], 0, v[88:89]
	global_store_dwordx4 v[8:9], v[12:15], off nt
	ds_read2_b32 v[8:9], v205 offset0:56 offset1:121
	v_lshl_add_u64 v[6:7], v[6:7], 0, v[90:91]
	s_waitcnt lgkmcnt(0)
	v_cvt_pk_bf16_f32 v12, v8, v9
	ds_read2_b32 v[8:9], v205 offset0:186 offset1:251
	s_waitcnt lgkmcnt(0)
	v_cvt_pk_bf16_f32 v13, v8, v9
	ds_read2_b32 v[8:9], v0 offset0:60 offset1:125
	s_waitcnt lgkmcnt(0)
	v_cvt_pk_bf16_f32 v14, v8, v9
	ds_read2_b32 v[8:9], v0 offset0:190 offset1:255
	s_waitcnt lgkmcnt(0)
	v_cvt_pk_bf16_f32 v15, v8, v9
	global_store_dwordx4 v[6:7], v[12:15], off nt
	s_waitcnt lgkmcnt(0)
	v_pk_add_f32 v[34:35], v[134:135], v[34:35]
	s_mov_b64 s[40:41], 0
	v_pk_add_f32 v[34:35], v[136:137], v[34:35]
